# NORM_A row loop: next-row loads kept in flight during compute (in-loop vmcnt(0) removed, unpack moved to loop bottom with counted waits)
# speedup vs baseline: 1.0037x; 1.0037x over previous
.LBB0_1407:
	v_readlane_b32 s0, v254, 16
	v_readlane_b32 s1, v254, 17
	s_cmp_lt_i32 s0, 9
	s_cselect_b64 s[0:1], -1, 0
	s_and_b64 s[4:5], s[0:1], s[4:5]
	s_andn2_b64 vcc, exec, s[4:5]
	s_cbranch_vccnz .LBB0_1415
	s_cmpk_gt_i32 s84, 0x7fff
	s_movk_i32 s18, 0x7fff
	s_cbranch_scc1 .LBB0_1415
	s_ashr_i32 s85, s84, 31
	s_lshl_b64 s[0:1], s[84:85], 12
	s_add_u32 s6, s2, s0
	s_addc_u32 s7, s3, s1
	v_lshlrev_b32_e32 v1, 3, v236
	s_waitcnt vmcnt(0)
	v_lshlrev_b32_e32 v98, 4, v236
	v_mov_b32_e32 v99, 0
	global_load_dwordx2 v[34:35], v1, s[6:7] nt
	global_load_dwordx2 v[36:37], v1, s[6:7] offset:512 nt
	global_load_dwordx2 v[38:39], v1, s[6:7] offset:1024 nt
	global_load_dwordx2 v[40:41], v1, s[6:7] offset:1536 nt
	global_load_dwordx2 v[42:43], v1, s[6:7] offset:2048 nt
	global_load_dwordx2 v[44:45], v1, s[6:7] offset:2560 nt
	global_load_dwordx2 v[46:47], v1, s[6:7] offset:3072 nt
	global_load_dwordx2 v[48:49], v1, s[6:7] offset:3584 nt
	s_mov_b64 s[6:7], 0x2000
	v_lshl_add_u64 v[18:19], s[90:91], 0, v[98:99]
	v_lshl_add_u64 v[20:21], v[18:19], 0, s[6:7]
	v_add_co_u32_e32 v22, vcc, 0x2000, v18
	s_lshl_b64 s[6:7], s[84:85], 13
	s_nop 0
	v_addc_co_u32_e32 v23, vcc, 0, v19, vcc
	s_add_u32 s6, s88, s6
	v_add_co_u32_e32 v50, vcc, 0x3000, v18
	s_addc_u32 s7, s89, s7
	s_movk_i32 s8, 0x1000
	v_addc_co_u32_e32 v51, vcc, 0, v19, vcc
	v_lshl_add_u64 v[26:27], s[6:7], 0, v[98:99]
	global_load_dwordx4 v[2:5], v[20:21], off offset:1024
	global_load_dwordx4 v[6:9], v[20:21], off offset:2048
	global_load_dwordx4 v[10:13], v[22:23], off
	global_load_dwordx4 v[14:17], v[20:21], off offset:3072
	s_nop 0
	global_load_dwordx4 v[18:21], v[50:51], off
	global_load_dwordx4 v[22:25], v[50:51], off offset:1024
	global_load_dwordx4 v[94:97], v98, s[6:7] nt
	global_load_dwordx4 v[90:93], v98, s[6:7] offset:1024 nt
	global_load_dwordx4 v[86:89], v98, s[6:7] offset:2048 nt
	global_load_dwordx4 v[82:85], v98, s[6:7] offset:3072 nt
	v_add_co_u32_e32 v52, vcc, s8, v26
	s_lshl_b64 s[6:7], s[84:85], 2
	s_nop 0
	v_addc_co_u32_e32 v53, vcc, 0, v27, vcc
	global_load_dwordx4 v[78:81], v[52:53], off nt
	global_load_dwordx4 v[74:77], v[52:53], off offset:1024 nt
	global_load_dwordx4 v[70:73], v[52:53], off offset:2048 nt
	global_load_dwordx4 v[66:69], v[52:53], off offset:3072 nt
	global_load_dwordx4 v[26:29], v[50:51], off offset:2048
	global_load_dwordx4 v[30:33], v[50:51], off offset:3072
	s_add_u32 s20, s6, 0x300000
	s_addc_u32 s21, s7, 0
	v_or_b32_e32 v100, s0, v1
	s_add_i32 s0, s84, s66
	s_ashr_i32 s67, s66, 31
	v_mov_b32_e32 v101, s1
	s_ashr_i32 s1, s0, 31
	s_lshl_b64 s[6:7], s[66:67], 2
	s_lshl_b64 s[10:11], s[66:67], 12
	s_lshl_b64 s[12:13], s[0:1], 13
	s_add_u32 s12, s88, s12
	s_addc_u32 s13, s89, s13
	s_lshl_b64 s[0:1], s[0:1], 12
	s_mov_b32 s19, 0xffff0000
	v_cmp_eq_u32_e64 s[8:9], 0, v236
	v_or_b32_e32 v104, s0, v1
	v_mov_b32_e32 v105, s1
	v_mov_b32_e32 v1, 0x358637bd
	s_mov_b32 s22, 0xf800000
	s_mov_b32 s23, 0x5b200000
	v_mov_b32_e32 v138, 0x3a000000
	s_mov_b32 s24, s84
	s_waitcnt vmcnt(23)
	v_lshlrev_b32_e32 v134, 16, v34
	v_and_b32_e32 v135, 0xffff0000, v34
	v_lshlrev_b32_e32 v136, 16, v35
	v_and_b32_e32 v137, 0xffff0000, v35
	v_lshl_add_u64 v[34:35], s[12:13], 0, v[98:99]
	s_mov_b64 s[12:13], 0x1000
	s_waitcnt vmcnt(22)
	v_lshlrev_b32_e32 v130, 16, v36
	v_and_b32_e32 v131, 0xffff0000, v36
	v_lshlrev_b32_e32 v132, 16, v37
	v_and_b32_e32 v133, 0xffff0000, v37
	s_waitcnt vmcnt(21)
	v_lshlrev_b32_e32 v126, 16, v38
	v_and_b32_e32 v127, 0xffff0000, v38
	v_lshlrev_b32_e32 v128, 16, v39
	v_and_b32_e32 v129, 0xffff0000, v39
	s_waitcnt vmcnt(20)
	v_lshlrev_b32_e32 v122, 16, v40
	v_and_b32_e32 v123, 0xffff0000, v40
	v_lshlrev_b32_e32 v124, 16, v41
	v_and_b32_e32 v125, 0xffff0000, v41
	s_waitcnt vmcnt(19)
	v_lshlrev_b32_e32 v118, 16, v42
	v_and_b32_e32 v119, 0xffff0000, v42
	v_lshlrev_b32_e32 v120, 16, v43
	v_and_b32_e32 v121, 0xffff0000, v43
	s_waitcnt vmcnt(18)
	v_lshlrev_b32_e32 v114, 16, v44
	v_and_b32_e32 v115, 0xffff0000, v44
	v_lshlrev_b32_e32 v116, 16, v45
	v_and_b32_e32 v117, 0xffff0000, v45
	s_waitcnt vmcnt(17)
	v_lshlrev_b32_e32 v110, 16, v46
	v_and_b32_e32 v111, 0xffff0000, v46
	v_lshlrev_b32_e32 v112, 16, v47
	v_and_b32_e32 v113, 0xffff0000, v47
	s_waitcnt vmcnt(16)
	v_lshlrev_b32_e32 v106, 16, v48
	v_and_b32_e32 v107, 0xffff0000, v48
	v_lshlrev_b32_e32 v108, 16, v49
	v_and_b32_e32 v109, 0xffff0000, v49
	v_lshl_add_u64 v[102:103], v[34:35], 0, s[12:13]
	s_waitcnt vmcnt(9)
	v_mov_b64_e32 v[34:35], v[94:95]
	s_waitcnt vmcnt(8)
	v_mov_b64_e32 v[38:39], v[90:91]
	s_waitcnt vmcnt(7)
	v_mov_b64_e32 v[42:43], v[86:87]
	s_waitcnt vmcnt(6)
	v_mov_b64_e32 v[46:47], v[82:83]
	s_waitcnt vmcnt(5)
	v_mov_b64_e32 v[50:51], v[78:79]
	s_waitcnt vmcnt(4)
	v_mov_b64_e32 v[54:55], v[74:75]
	s_waitcnt vmcnt(3)
	v_mov_b64_e32 v[58:59], v[70:71]
	s_waitcnt vmcnt(2)
	v_mov_b64_e32 v[62:63], v[66:67]
	s_lshl_b64 s[12:13], s[66:67], 13
	v_mov_b32_e32 v98, 0x260
	v_mov_b64_e32 v[36:37], v[96:97]
	v_mov_b64_e32 v[40:41], v[92:93]
	v_mov_b64_e32 v[44:45], v[88:89]
	v_mov_b64_e32 v[48:49], v[84:85]
	v_mov_b64_e32 v[52:53], v[80:81]
	v_mov_b64_e32 v[56:57], v[76:77]
	v_mov_b64_e32 v[60:61], v[72:73]
	v_mov_b64_e32 v[64:65], v[68:69]
	s_waitcnt vmcnt(0)
	s_branch .LBB0_1411
.LBB0_1410:
	s_or_b64 exec, exec, s[16:17]
	s_and_b64 vcc, exec, s[14:15]
	s_cbranch_vccnz .Lna_no_next
	s_waitcnt vmcnt(23)
	v_lshlrev_b32_e32 v139, 16, v142
	v_and_b32_e32 v140, 0xffff0000, v142
	v_lshlrev_b32_e32 v141, 16, v143
	v_and_b32_e32 v142, 0xffff0000, v143
	s_waitcnt vmcnt(22)
	v_lshlrev_b32_e32 v143, 16, v146
	v_and_b32_e32 v144, 0xffff0000, v146
	v_lshlrev_b32_e32 v145, 16, v147
	v_and_b32_e32 v146, 0xffff0000, v147
	s_waitcnt vmcnt(21)
	v_lshlrev_b32_e32 v147, 16, v150
	v_and_b32_e32 v148, 0xffff0000, v150
	v_lshlrev_b32_e32 v149, 16, v151
	v_and_b32_e32 v150, 0xffff0000, v151
	s_waitcnt vmcnt(20)
	v_lshlrev_b32_e32 v151, 16, v154
	v_and_b32_e32 v152, 0xffff0000, v154
	v_lshlrev_b32_e32 v153, 16, v155
	v_and_b32_e32 v154, 0xffff0000, v155
	s_waitcnt vmcnt(19)
	v_lshlrev_b32_e32 v155, 16, v158
	v_and_b32_e32 v156, 0xffff0000, v158
	v_lshlrev_b32_e32 v157, 16, v159
	v_and_b32_e32 v158, 0xffff0000, v159
	s_waitcnt vmcnt(18)
	v_lshlrev_b32_e32 v159, 16, v162
	v_and_b32_e32 v160, 0xffff0000, v162
	v_lshlrev_b32_e32 v161, 16, v163
	v_and_b32_e32 v162, 0xffff0000, v163
	s_waitcnt vmcnt(17)
	v_lshlrev_b32_e32 v163, 16, v166
	v_and_b32_e32 v164, 0xffff0000, v166
	v_lshlrev_b32_e32 v165, 16, v167
	v_and_b32_e32 v166, 0xffff0000, v167
	s_waitcnt vmcnt(12)
	v_lshlrev_b32_e32 v167, 16, v170
	v_and_b32_e32 v168, 0xffff0000, v170
	v_lshlrev_b32_e32 v169, 16, v171
	v_and_b32_e32 v170, 0xffff0000, v171
	s_waitcnt vmcnt(8)
.Lna_no_next:
	s_add_u32 s20, s20, s6
	v_mov_b64_e32 v[96:97], v[36:37]
	v_mov_b64_e32 v[92:93], v[40:41]
	v_mov_b64_e32 v[88:89], v[44:45]
	v_mov_b64_e32 v[84:85], v[48:49]
	v_mov_b64_e32 v[80:81], v[52:53]
	v_mov_b64_e32 v[76:77], v[56:57]
	v_mov_b64_e32 v[72:73], v[60:61]
	v_mov_b64_e32 v[68:69], v[64:65]
	s_addc_u32 s21, s21, s7
	v_lshl_add_u64 v[100:101], v[100:101], 0, s[10:11]
	v_lshl_add_u64 v[102:103], v[102:103], 0, s[12:13]
	v_lshl_add_u64 v[104:105], v[104:105], 0, s[10:11]
	s_andn2_b64 vcc, exec, s[14:15]
	v_mov_b64_e32 v[94:95], v[34:35]
	v_mov_b64_e32 v[90:91], v[38:39]
	v_mov_b64_e32 v[86:87], v[42:43]
	v_mov_b64_e32 v[82:83], v[46:47]
	v_mov_b64_e32 v[78:79], v[50:51]
	v_mov_b64_e32 v[74:75], v[54:55]
	v_mov_b64_e32 v[70:71], v[58:59]
	v_mov_b64_e32 v[66:67], v[62:63]
	v_mov_b32_e32 v134, v139
	v_mov_b32_e32 v135, v140
	v_mov_b32_e32 v136, v141
	v_mov_b32_e32 v137, v142
	v_mov_b32_e32 v130, v143
	v_mov_b32_e32 v131, v144
	v_mov_b32_e32 v132, v145
	v_mov_b32_e32 v133, v146
	v_mov_b32_e32 v126, v147
	v_mov_b32_e32 v127, v148
	v_mov_b32_e32 v128, v149
	v_mov_b32_e32 v129, v150
	v_mov_b32_e32 v122, v151
	v_mov_b32_e32 v123, v152
	v_mov_b32_e32 v124, v153
	v_mov_b32_e32 v125, v154
	v_mov_b32_e32 v118, v155
	v_mov_b32_e32 v119, v156
	v_mov_b32_e32 v120, v157
	v_mov_b32_e32 v121, v158
	v_mov_b32_e32 v114, v159
	v_mov_b32_e32 v115, v160
	v_mov_b32_e32 v116, v161
	v_mov_b32_e32 v117, v162
	v_mov_b32_e32 v110, v163
	v_mov_b32_e32 v111, v164
	v_mov_b32_e32 v112, v165
	v_mov_b32_e32 v113, v166
	v_mov_b32_e32 v106, v167
	v_mov_b32_e32 v107, v168
	v_mov_b32_e32 v108, v169
	v_mov_b32_e32 v109, v170
	s_cbranch_vccz .LBB0_1415

.LBB0_1413:
	v_mul_f32_e32 v177, v135, v135
	v_mul_f32_e32 v172, v137, v137
	v_fmac_f32_e32 v177, v134, v134
	v_fmac_f32_e32 v172, v136, v136
	v_add_f32_e32 v177, v177, v172
	v_mul_f32_e32 v172, v131, v131
	v_mul_f32_e32 v173, v133, v133
	v_fmac_f32_e32 v172, v130, v130
	v_fmac_f32_e32 v173, v132, v132
	v_add_f32_e32 v172, v172, v173
	v_add_f32_e32 v177, v177, v172
	v_mul_f32_e32 v172, v127, v127
	v_mul_f32_e32 v173, v129, v129
	v_fmac_f32_e32 v172, v126, v126
	v_fmac_f32_e32 v173, v128, v128
	v_add_f32_e32 v172, v172, v173
	v_add_f32_e32 v177, v177, v172
	v_mul_f32_e32 v172, v123, v123
	v_mul_f32_e32 v173, v125, v125
	v_fmac_f32_e32 v172, v122, v122
	v_fmac_f32_e32 v173, v124, v124
	v_add_f32_e32 v172, v172, v173
	v_add_f32_e32 v177, v177, v172
	v_mul_f32_e32 v172, v119, v119
	v_mul_f32_e32 v173, v121, v121
	v_fmac_f32_e32 v172, v118, v118
	v_fmac_f32_e32 v173, v120, v120
	v_add_f32_e32 v172, v172, v173
	v_add_f32_e32 v177, v177, v172
	v_mul_f32_e32 v172, v115, v115
	v_mul_f32_e32 v173, v117, v117
	v_fmac_f32_e32 v172, v114, v114
	v_fmac_f32_e32 v173, v116, v116
	v_add_f32_e32 v172, v172, v173
	v_add_f32_e32 v177, v177, v172
	v_mul_f32_e32 v172, v111, v111
	v_mul_f32_e32 v173, v113, v113
	v_fmac_f32_e32 v172, v110, v110
	v_fmac_f32_e32 v173, v112, v112
	v_add_f32_e32 v172, v172, v173
	v_add_f32_e32 v177, v177, v172
	v_mul_f32_e32 v172, v107, v107
	v_mul_f32_e32 v173, v109, v109
	v_fmac_f32_e32 v172, v106, v106
	v_fmac_f32_e32 v173, v108, v108
	v_add_f32_e32 v172, v172, v173
	v_add_f32_e32 v177, v177, v172
	v_mov_b32_e32 v172, 0
	s_nop 0
	v_add_f32_dpp v177, v177, v177 quad_perm:[1,0,3,2] row_mask:0xf bank_mask:0xf bound_ctrl:1
	s_nop 1
	v_add_f32_dpp v177, v177, v177 quad_perm:[2,3,0,1] row_mask:0xf bank_mask:0xf bound_ctrl:1
	s_nop 1
	v_add_f32_dpp v177, v177, v177 row_half_mirror row_mask:0xf bank_mask:0xf bound_ctrl:1
	s_nop 1
	v_add_f32_dpp v177, v177, v177 row_mirror row_mask:0xf bank_mask:0xf bound_ctrl:1
	s_nop 1
	v_mov_b32_dpp v172, v177 row_bcast:15 row_mask:0xa bank_mask:0xf
	v_add_f32_e32 v177, v177, v172
	v_mov_b32_e32 v172, 0
	s_nop 1
	v_mov_b32_dpp v172, v177 row_bcast:31 row_mask:0xc bank_mask:0xf
	v_add_f32_e32 v177, v177, v172
	s_nop 0
	v_readlane_b32 s0, v177, 63
	s_nop 1
	v_fma_f32 v177, s0, v138, v1
	v_mul_f32_e32 v172, 0x4f800000, v177
	v_cmp_gt_f32_e32 vcc, s22, v177
	s_nop 1
	v_cndmask_b32_e32 v177, v177, v172, vcc
	v_sqrt_f32_e32 v172, v177
	s_nop 0
	v_add_u32_e32 v173, -1, v172
	v_fma_f32 v174, -v173, v172, v177
	v_cmp_ge_f32_e64 s[0:1], 0, v174
	v_add_u32_e32 v174, 1, v172
	s_nop 0
	v_cndmask_b32_e64 v173, v172, v173, s[0:1]
	v_fma_f32 v172, -v174, v172, v177
	v_cmp_lt_f32_e64 s[0:1], 0, v172
	s_nop 1
	v_cndmask_b32_e64 v172, v173, v174, s[0:1]
	v_mul_f32_e32 v173, 0x37800000, v172
	v_cndmask_b32_e32 v172, v172, v173, vcc
	v_cmp_class_f32_e32 vcc, v177, v98
	s_nop 1
	v_cndmask_b32_e32 v177, v172, v177, vcc
	v_div_scale_f32 v172, s[0:1], v177, v177, 1.0
	v_rcp_f32_e32 v173, v172
	s_nop 0
	v_fma_f32 v174, -v172, v173, 1.0
	v_fmac_f32_e32 v173, v174, v173
	v_div_scale_f32 v174, vcc, 1.0, v177, 1.0
	v_mul_f32_e32 v175, v174, v173
	v_fma_f32 v176, -v172, v175, v174
	v_fmac_f32_e32 v175, v176, v173
	v_fma_f32 v172, -v172, v175, v174
	v_div_fmas_f32 v172, v172, v173, v175
	v_div_fixup_f32 v172, v172, v177, 1.0
	v_pk_mul_f32 v[134:135], v[172:173], v[134:135] op_sel_hi:[0,1]
	v_pk_fma_f32 v[94:95], v[134:135], v[10:11], v[94:95]
	v_pk_mul_f32 v[108:109], v[172:173], v[108:109] op_sel_hi:[0,1]
	v_pk_fma_f32 v[68:69], v[108:109], v[32:33], v[68:69]
	v_bfe_u32 v108, v94, 16, 1
	v_pk_mul_f32 v[136:137], v[172:173], v[136:137] op_sel_hi:[0,1]
	v_add3_u32 v108, v94, v108, s18
	v_bfe_u32 v109, v95, 16, 1
	v_pk_fma_f32 v[96:97], v[136:137], v[12:13], v[96:97]
	v_lshrrev_b32_e32 v108, 16, v108
	v_add3_u32 v109, v95, v109, s18
	v_pk_mul_f32 v[110:111], v[172:173], v[110:111] op_sel_hi:[0,1]
	v_pk_mul_f32 v[106:107], v[172:173], v[106:107] op_sel_hi:[0,1]
	v_and_or_b32 v108, v109, s19, v108
	v_bfe_u32 v109, v96, 16, 1
	v_pk_fma_f32 v[70:71], v[110:111], v[26:27], v[70:71]
	v_pk_fma_f32 v[66:67], v[106:107], v[30:31], v[66:67]
	v_lshl_add_u64 v[106:107], s[86:87], 0, v[100:101]
	v_add3_u32 v109, v96, v109, s18
	v_bfe_u32 v110, v97, 16, 1
	v_pk_mul_f32 v[130:131], v[172:173], v[130:131] op_sel_hi:[0,1]
	v_lshrrev_b32_e32 v109, 16, v109
	v_add3_u32 v110, v97, v110, s18
	v_add_co_u32_e32 v106, vcc, s23, v106
	v_pk_fma_f32 v[90:91], v[130:131], v[2:3], v[90:91]
	v_and_or_b32 v109, v110, s19, v109
	v_addc_co_u32_e32 v107, vcc, 0, v107, vcc
	global_store_dwordx2 v[106:107], v[108:109], off
	v_bfe_u32 v108, v90, 16, 1
	v_pk_mul_f32 v[132:133], v[172:173], v[132:133] op_sel_hi:[0,1]
	v_add3_u32 v108, v90, v108, s18
	v_bfe_u32 v109, v91, 16, 1
	v_pk_fma_f32 v[92:93], v[132:133], v[4:5], v[92:93]
	v_lshrrev_b32_e32 v108, 16, v108
	v_add3_u32 v109, v91, v109, s18
	v_and_or_b32 v108, v109, s19, v108
	v_bfe_u32 v109, v92, 16, 1
	v_add3_u32 v109, v92, v109, s18
	v_bfe_u32 v110, v93, 16, 1
	v_pk_mul_f32 v[126:127], v[172:173], v[126:127] op_sel_hi:[0,1]
	v_lshrrev_b32_e32 v109, 16, v109
	v_add3_u32 v110, v93, v110, s18
	v_pk_fma_f32 v[86:87], v[126:127], v[6:7], v[86:87]
	v_and_or_b32 v109, v110, s19, v109
	global_store_dwordx2 v[106:107], v[108:109], off offset:512
	v_bfe_u32 v108, v86, 16, 1
	v_pk_mul_f32 v[128:129], v[172:173], v[128:129] op_sel_hi:[0,1]
	v_add3_u32 v108, v86, v108, s18
	v_bfe_u32 v109, v87, 16, 1
	v_pk_fma_f32 v[88:89], v[128:129], v[8:9], v[88:89]
	v_lshrrev_b32_e32 v108, 16, v108
	v_add3_u32 v109, v87, v109, s18
	v_and_or_b32 v108, v109, s19, v108
	v_bfe_u32 v109, v88, 16, 1
	v_add3_u32 v109, v88, v109, s18
	v_bfe_u32 v110, v89, 16, 1
	v_pk_mul_f32 v[122:123], v[172:173], v[122:123] op_sel_hi:[0,1]
	v_lshrrev_b32_e32 v109, 16, v109
	v_add3_u32 v110, v89, v110, s18
	v_pk_fma_f32 v[82:83], v[122:123], v[14:15], v[82:83]
	v_and_or_b32 v109, v110, s19, v109
	global_store_dwordx2 v[106:107], v[108:109], off offset:1024
	v_bfe_u32 v108, v82, 16, 1
	v_pk_mul_f32 v[124:125], v[172:173], v[124:125] op_sel_hi:[0,1]
	v_add3_u32 v108, v82, v108, s18
	v_bfe_u32 v109, v83, 16, 1
	v_pk_fma_f32 v[84:85], v[124:125], v[16:17], v[84:85]
	v_lshrrev_b32_e32 v108, 16, v108
	v_add3_u32 v109, v83, v109, s18
	v_and_or_b32 v108, v109, s19, v108
	v_bfe_u32 v109, v84, 16, 1
	v_add3_u32 v109, v84, v109, s18
	v_bfe_u32 v110, v85, 16, 1
	v_pk_mul_f32 v[118:119], v[172:173], v[118:119] op_sel_hi:[0,1]
	v_lshrrev_b32_e32 v109, 16, v109
	v_add3_u32 v110, v85, v110, s18
	v_pk_fma_f32 v[78:79], v[118:119], v[18:19], v[78:79]
	v_and_or_b32 v109, v110, s19, v109
	global_store_dwordx2 v[106:107], v[108:109], off offset:1536
	v_bfe_u32 v108, v78, 16, 1
	v_pk_mul_f32 v[120:121], v[172:173], v[120:121] op_sel_hi:[0,1]
	v_add3_u32 v108, v78, v108, s18
	v_bfe_u32 v109, v79, 16, 1
	v_pk_fma_f32 v[80:81], v[120:121], v[20:21], v[80:81]
	v_lshrrev_b32_e32 v108, 16, v108
	v_add3_u32 v109, v79, v109, s18
	v_and_or_b32 v108, v109, s19, v108
	v_bfe_u32 v109, v80, 16, 1
	v_add3_u32 v109, v80, v109, s18
	v_bfe_u32 v110, v81, 16, 1
	v_pk_mul_f32 v[114:115], v[172:173], v[114:115] op_sel_hi:[0,1]
	v_lshrrev_b32_e32 v109, 16, v109
	v_add3_u32 v110, v81, v110, s18
	v_pk_fma_f32 v[74:75], v[114:115], v[22:23], v[74:75]
	v_and_or_b32 v109, v110, s19, v109
	global_store_dwordx2 v[106:107], v[108:109], off offset:2048
	v_bfe_u32 v108, v74, 16, 1
	v_pk_mul_f32 v[116:117], v[172:173], v[116:117] op_sel_hi:[0,1]
	v_add3_u32 v108, v74, v108, s18
	v_bfe_u32 v109, v75, 16, 1
	v_pk_fma_f32 v[76:77], v[116:117], v[24:25], v[76:77]
	v_lshrrev_b32_e32 v108, 16, v108
	v_add3_u32 v109, v75, v109, s18
	v_and_or_b32 v108, v109, s19, v108
	v_bfe_u32 v109, v76, 16, 1
	v_add3_u32 v109, v76, v109, s18
	v_bfe_u32 v110, v77, 16, 1
	v_lshrrev_b32_e32 v109, 16, v109
	v_add3_u32 v110, v77, v110, s18
	v_and_or_b32 v109, v110, s19, v109
	global_store_dwordx2 v[106:107], v[108:109], off offset:2560
	v_bfe_u32 v108, v70, 16, 1
	v_pk_mul_f32 v[112:113], v[172:173], v[112:113] op_sel_hi:[0,1]
	v_add3_u32 v108, v70, v108, s18
	v_bfe_u32 v109, v71, 16, 1
	v_pk_fma_f32 v[72:73], v[112:113], v[28:29], v[72:73]
	v_lshrrev_b32_e32 v108, 16, v108
	v_add3_u32 v109, v71, v109, s18
	v_mul_f32_e32 v95, v95, v95
	v_mul_f32_e32 v91, v91, v91
	v_and_or_b32 v108, v109, s19, v108
	v_bfe_u32 v109, v72, 16, 1
	v_fmac_f32_e32 v95, v94, v94
	v_mul_f32_e32 v94, v97, v97
	v_fmac_f32_e32 v91, v90, v90
	v_mul_f32_e32 v90, v93, v93
	v_mul_f32_e32 v87, v87, v87
	v_add3_u32 v109, v72, v109, s18
	v_bfe_u32 v110, v73, 16, 1
	v_fmac_f32_e32 v94, v96, v96
	v_fmac_f32_e32 v90, v92, v92
	v_fmac_f32_e32 v87, v86, v86
	v_mul_f32_e32 v86, v89, v89
	v_mul_f32_e32 v83, v83, v83
	v_lshrrev_b32_e32 v109, 16, v109
	v_add3_u32 v110, v73, v110, s18
	v_add_f32_e32 v94, v95, v94
	v_add_f32_e32 v90, v91, v90
	v_fmac_f32_e32 v86, v88, v88
	v_fmac_f32_e32 v83, v82, v82
	v_mul_f32_e32 v82, v85, v85
	v_mul_f32_e32 v79, v79, v79
	v_and_or_b32 v109, v110, s19, v109
	v_add_f32_e32 v90, v94, v90
	v_add_f32_e32 v86, v87, v86
	v_fmac_f32_e32 v82, v84, v84
	v_fmac_f32_e32 v79, v78, v78
	v_mul_f32_e32 v78, v81, v81
	v_mul_f32_e32 v75, v75, v75
	global_store_dwordx2 v[106:107], v[108:109], off offset:3072
	v_bfe_u32 v109, v67, 16, 1
	v_add_f32_e32 v86, v90, v86
	v_add_f32_e32 v82, v83, v82
	v_fmac_f32_e32 v78, v80, v80
	v_fmac_f32_e32 v75, v74, v74
	v_mul_f32_e32 v74, v77, v77
	v_mul_f32_e32 v71, v71, v71
	v_bfe_u32 v108, v66, 16, 1
	v_add3_u32 v109, v67, v109, s18
	v_add_f32_e32 v82, v86, v82
	v_add_f32_e32 v78, v79, v78
	v_fmac_f32_e32 v74, v76, v76
	v_fmac_f32_e32 v71, v70, v70
	v_mul_f32_e32 v70, v73, v73
	v_mul_f32_e32 v67, v67, v67
	v_add3_u32 v108, v66, v108, s18
	v_add_f32_e32 v78, v82, v78
	v_add_f32_e32 v74, v75, v74
	v_fmac_f32_e32 v70, v72, v72
	v_fmac_f32_e32 v67, v66, v66
	v_mul_f32_e32 v66, v69, v69
	v_add_f32_e32 v74, v78, v74
	v_add_f32_e32 v70, v71, v70
	v_fmac_f32_e32 v66, v68, v68
	v_add_f32_e32 v70, v74, v70
	v_add_f32_e32 v66, v67, v66
	v_add_f32_e32 v66, v70, v66
	v_mov_b32_e32 v67, 0
	v_lshrrev_b32_e32 v108, 16, v108
	v_add_f32_dpp v66, v66, v66 quad_perm:[1,0,3,2] row_mask:0xf bank_mask:0xf bound_ctrl:1
	v_and_or_b32 v108, v109, s19, v108
	v_bfe_u32 v109, v68, 16, 1
	v_add_f32_dpp v66, v66, v66 quad_perm:[2,3,0,1] row_mask:0xf bank_mask:0xf bound_ctrl:1
	v_add3_u32 v109, v68, v109, s18
	v_bfe_u32 v110, v69, 16, 1
	v_add_f32_dpp v66, v66, v66 row_half_mirror row_mask:0xf bank_mask:0xf bound_ctrl:1
	v_lshrrev_b32_e32 v109, 16, v109
	v_add3_u32 v110, v69, v110, s18
	v_add_f32_dpp v66, v66, v66 row_mirror row_mask:0xf bank_mask:0xf bound_ctrl:1
	v_and_or_b32 v109, v110, s19, v109
	global_store_dwordx2 v[106:107], v[108:109], off offset:3584
	v_mov_b32_dpp v67, v66 row_bcast:15 row_mask:0xa bank_mask:0xf
	v_add_f32_e32 v66, v66, v67
	v_mov_b32_e32 v67, 0
	s_nop 1
	v_mov_b32_dpp v67, v66 row_bcast:31 row_mask:0xc bank_mask:0xf
	v_add_f32_e32 v66, v66, v67
	s_nop 0
	v_readlane_b32 s0, v66, 63
	s_and_saveexec_b64 s[16:17], s[8:9]
	s_cbranch_execz .LBB0_1410
	v_fma_f32 v66, s0, v138, v1
	v_mul_f32_e32 v67, 0x4f800000, v66
	v_cmp_gt_f32_e32 vcc, s22, v66
	s_nop 1
	v_cndmask_b32_e32 v66, v66, v67, vcc
	v_sqrt_f32_e32 v67, v66
	s_nop 0
	v_add_u32_e32 v68, -1, v67
	v_fma_f32 v70, -v68, v67, v66
	v_add_u32_e32 v69, 1, v67
	v_cmp_ge_f32_e64 s[0:1], 0, v70
	s_nop 1
	v_cndmask_b32_e64 v68, v67, v68, s[0:1]
	v_fma_f32 v67, -v69, v67, v66
	v_cmp_lt_f32_e64 s[0:1], 0, v67
	s_nop 1
	v_cndmask_b32_e64 v67, v68, v69, s[0:1]
	v_mul_f32_e32 v68, 0x37800000, v67
	v_cndmask_b32_e32 v67, v67, v68, vcc
	v_cmp_class_f32_e32 vcc, v66, v98
	s_nop 1
	v_cndmask_b32_e32 v66, v67, v66, vcc
	v_div_scale_f32 v67, s[0:1], v66, v66, 1.0
	v_rcp_f32_e32 v68, v67
	s_add_u32 s0, s86, s20
	s_addc_u32 s1, s87, s21
	v_fma_f32 v69, -v67, v68, 1.0
	v_fmac_f32_e32 v68, v69, v68
	v_div_scale_f32 v69, vcc, 1.0, v66, 1.0
	v_mul_f32_e32 v70, v69, v68
	v_fma_f32 v71, -v67, v70, v69
	v_fmac_f32_e32 v70, v71, v68
	v_fma_f32 v67, -v67, v70, v69
	v_div_fmas_f32 v67, v67, v68, v70
	v_div_fixup_f32 v66, v67, v66, 1.0
	global_store_dword v99, v66, s[0:1]
	s_branch .LBB0_1410
